# static s_setprio 1 for waves 4-7 during phase 3 (attention + HGRN), on top of sc1/nt policy variant
# speedup vs baseline: 1.0068x; 1.0068x over previous
.LBB0_640:
	s_add_u32 s0, s96, 0x17400000
	s_addc_u32 s1, s97, 0
	s_add_u32 s82, s96, 0x7400000
	s_addc_u32 s83, s97, 0
	v_writelane_b32 v254, s0, 57
	s_cmp_lt_i32 s48, 4
	v_lshlrev_b32_e32 v253, 4, v0
	v_writelane_b32 v254, s1, 58
	s_cselect_b64 s[0:1], -1, 0
	s_cmp_gt_i32 s49, 3
	s_cselect_b64 s[2:3], -1, 0
	s_and_b64 s[0:1], s[0:1], s[2:3]
	s_andn2_b64 vcc, exec, s[0:1]
	v_lshlrev_b32_e32 v179, 3, v0
	v_mbcnt_lo_u32_b32 v252, -1, 0
	s_cbranch_vccnz .LBB0_974
	v_readlane_b32 s0, v254, 44
	s_nop 3
	s_cmp_lt_u32 s0, 4
	s_cbranch_scc1 .Lprio_skip
	s_setprio 1
.Lprio_skip:
	v_and_b32_e32 v124, 0x7f, v0
	v_lshlrev_b32_e32 v11, 2, v124
	s_add_i32 s4, 0, 0x1c000
	v_readlane_b32 s5, v254, 44
	v_lshrrev_b32_e32 v165, 4, v1
	v_and_b32_e32 v5, 0xf0, v253
	s_add_i32 s0, 0, 0x1ca00
	v_lshlrev_b32_e32 v8, 1, v124
	v_add_u32_e32 v133, s4, v11
	s_lshr_b32 s10, s69, 7
	s_lshl_b32 s4, s5, 1
	v_and_b32_e32 v164, 15, v0
	v_lshrrev_b32_e32 v4, 4, v0
	v_add_u32_e32 v128, s0, v5
	v_add_u32_e32 v9, s0, v8
	s_add_i32 s0, 0, 0x1c200
	s_and_b32 s11, s4, 2
	s_lshl_b32 s4, s10, 4
	v_lshlrev_b32_e32 v130, 2, v165
	v_lshrrev_b32_e32 v3, 7, v0
	v_mul_u32_u24_e32 v2, 0x9000, v4
	v_lshrrev_b32_e32 v106, 3, v0
	s_add_i32 s3, 0, 0x13c00
	v_add_u32_e32 v132, s0, v11
	v_or_b32_e32 v11, s4, v130
	v_or_b32_e32 v12, s4, v164
	s_and_b32 s4, s69, 0xffffffc0
	v_or_b32_e32 v125, v2, v5
	v_mul_u32_u24_e32 v2, 0x9000, v106
	v_and_b32_e32 v108, 0x70, v253
	s_add_i32 s1, 0, 0x20a00
	v_lshlrev_b32_e32 v7, 12, v3
	s_lshl_b32 s33, s5, 5
	s_add_i32 s18, 0, 0x11800
	s_add_i32 s4, s4, s3
	v_mul_u32_u24_e32 v21, 0x1100, v3
	v_mul_u32_u24_e32 v22, 0x1200, v3
	v_lshl_or_b32 v3, v3, 4, 1
	v_lshl_or_b32 v2, v108, 1, v2
	s_movk_i32 s12, 0x110
	v_mov_b32_e32 v109, 0
	v_mul_u32_u24_e32 v23, 0x110, v3
	v_mul_u32_u24_e32 v24, 0x120, v3
	s_cmp_le_u32 s11, s10
	v_lshl_or_b32 v3, s11, 4, v164
	s_movk_i32 s13, 0x90
	v_or_b32_e32 v27, 1, v11
	v_or_b32_e32 v28, 2, v11
	v_or_b32_e32 v29, 3, v11
	v_or_b32_e32 v31, 16, v164
	v_readlane_b32 s40, v254, 23
	v_bfe_u32 v107, v0, 2, 2
	v_add_u32_e32 v127, 0x6000, v2
	v_lshlrev_b32_e32 v2, 2, v108
	v_mul_lo_u32 v12, v12, s12
	v_lshlrev_b32_e32 v135, 3, v165
	v_mad_u32_u24 v137, v164, s12, 0
	v_or_b32_e32 v20, 0x200, v0
	s_cselect_b64 s[34:35], -1, 0
	v_mul_u32_u24_e32 v25, 0x110, v3
	v_mul_lo_u32 v26, v11, s13
	s_cmp_lt_u32 s11, s10
	v_or_b32_e32 v30, 16, v3
	v_mad_u32_u24 v142, v31, s12, 0
	v_lshl_add_u32 v32, v3, 1, s18
	v_cmp_gt_u32_e64 s[10:11], v3, v11
	v_cmp_gt_u32_e64 s[12:13], v3, v27
	v_cmp_gt_u32_e64 s[14:15], v3, v28
	v_cmp_gt_u32_e64 s[16:17], v3, v29
	v_mov_b32_e32 v3, v109
	v_readlane_b32 s44, v254, 27
	v_readlane_b32 s45, v254, 28
	v_add_u32_e32 v6, s3, v2
	v_and_b32_e32 v13, 48, v0
	v_or_b32_e32 v14, v135, v107
	v_and_b32_e32 v136, 24, v179
	v_or_b32_e32 v17, 16, v130
	s_movk_i32 s3, 0x120
	v_lshrrev_b32_e32 v20, 4, v20
	v_lshl_add_u64 v[110:111], s[44:45], 0, v[2:3]
	v_lshl_add_u64 v[2:3], s[96:97], 0, v[108:109]
	s_mov_b64 s[26:27], 0x3400000
	v_lshl_or_b32 v108, v106, 11, v108
	v_add_u32_e32 v129, s1, v5
	v_add_u32_e32 v5, 0, v5
	v_add_u32_e32 v10, s1, v8
	v_add_u32_e32 v8, 0, v8
	s_movk_i32 s2, 0x80
	v_add_u32_e32 v12, 0, v12
	v_add_u32_e32 v134, 0, v13
	v_or_b32_e32 v15, s33, v136
	v_add_u32_e32 v16, s18, v13
	s_waitcnt vmcnt(1)
	v_lshl_add_u32 v18, v164, 2, s4
	s_waitcnt vmcnt(0)
	v_mul_u32_u24_e32 v19, 0x210, v106
	v_lshlrev_b32_e32 v138, 8, v4
	v_mul_u32_u24_e32 v4, 0x120, v4
	v_lshlrev_b32_e32 v139, 8, v20
	v_mul_u32_u24_e32 v20, 0x120, v20
	s_movk_i32 s4, 0xff
	s_movk_i32 s6, 0x17f
	s_movk_i32 s8, 0x1ff
	v_mad_u32_u24 v140, v14, s3, 0
	v_mul_u32_u24_e32 v14, 0x90, v164
	v_lshlrev_b32_e32 v141, 1, v17
	v_mul_u32_u24_e32 v31, 0x840, v165
	v_mul_u32_u24_e32 v17, 0x210, v17
	v_lshl_add_u32 v33, v30, 1, s18
	v_readlane_b32 s42, v254, 25
	v_readlane_b32 s43, v254, 26
	v_readlane_b32 s46, v254, 29
	v_readlane_b32 s47, v254, 30
	v_readlane_b32 s48, v254, 31
	v_lshl_add_u64 v[112:113], v[2:3], 0, s[26:27]
	v_lshl_add_u64 v[2:3], s[96:97], 0, v[108:109]
	s_mov_b64 s[26:27], 0x33e0000
	v_add_u32_e32 v126, 0x120000, v125
	s_mov_b32 s31, 0
	v_lshl_add_u32 v131, v0, 2, s0
	v_cmp_gt_u32_e64 s[0:1], s2, v0
	v_cmp_lt_u32_e64 s[4:5], s4, v0
	v_cmp_lt_u32_e64 s[6:7], s6, v0
	v_cmp_lt_u32_e64 s[8:9], s8, v0
	s_cselect_b64 s[36:37], -1, 0
	v_add_u32_e32 v143, 0x1100, v142
	v_add_u32_e32 v144, 0x2200, v142
	v_or_b32_e32 v145, 64, v135
	v_or_b32_e32 v146, 0x60, v135
	v_cmp_gt_u32_e64 s[18:19], v30, v11
	v_cmp_gt_u32_e64 s[20:21], v30, v27
	v_cmp_gt_u32_e64 s[22:23], v30, v28
	v_cmp_gt_u32_e64 s[24:25], v30, v29
	v_lshl_add_u64 v[114:115], v[2:3], 0, s[26:27]
	s_add_i32 s3, 0, 0x26400
	s_movk_i32 s42, 0x4000
	s_movk_i32 s43, 0x3000
	s_movk_i32 s44, 0x5000
	v_add_u32_e32 v147, v5, v4
	v_add_u32_e32 v148, v5, v20
	v_add_u32_e32 v149, v9, v7
	v_add_u32_e32 v150, v10, v7
	s_mov_b32 s45, 0x800000
	s_mov_b32 s46, 0x3f317217
	s_mov_b32 s47, 0x7f800000
	s_movk_i32 s48, 0x7fff
	v_add_u32_e32 v151, v8, v21
	v_add_u32_e32 v152, v8, v22
	v_add_u32_e32 v153, v8, v23
	v_add_u32_e32 v154, v8, v24
	v_add_u32_e32 v155, v32, v26
	v_add_u32_e32 v156, v33, v26
	v_add_u32_e32 v157, v140, v15
	v_add_u32_e32 v158, v16, v14
	v_add_u32_e32 v159, v18, v31
	v_add_u32_e32 v160, v18, v17
	v_add_u32_e32 v161, v6, v19
	v_mov_b32_e32 v162, 0x358637bd
	v_mov_b32_e32 v163, 0x41b17218
	v_add_u32_e32 v167, v12, v13
	v_add_u32_e32 v168, v134, v25
	v_mbcnt_hi_u32_b32 v166, -1, v252
	v_readlane_b32 s41, v254, 24
	v_readlane_b32 s49, v254, 32
	v_readlane_b32 s50, v254, 33
	v_readlane_b32 s51, v254, 34
	v_readlane_b32 s52, v254, 35
	v_readlane_b32 s53, v254, 36
	v_readlane_b32 s54, v254, 37
	v_readlane_b32 s55, v254, 38
	s_branch .LBB0_644

.LBB0_920:
	s_setprio 0
	v_readlane_b32 s48, v254, 53
	v_readlane_b32 s49, v254, 54
	s_cmp_lt_i32 s49, 5
	s_barrier
	s_cbranch_scc1 .LBB0_974
	s_waitcnt vmcnt(0)
	s_barrier
	s_mov_b64 s[0:1], exec
	v_readlane_b32 s2, v254, 5
	v_readlane_b32 s3, v254, 6
	s_and_b64 s[2:3], s[0:1], s[2:3]
	s_mov_b64 exec, s[2:3]
	s_cbranch_execz .LBB0_973
	s_add_i32 s2, 0, 0x26160
	v_mov_b32_e32 v2, s2
	s_waitcnt vmcnt(0) expcnt(0) lgkmcnt(0)
	ds_read_b32 v4, v2
	s_add_i32 s2, 0, 0x26164
	v_mov_b32_e32 v2, s2
	ds_read_b32 v2, v2
	s_waitcnt lgkmcnt(1)
	v_cmp_ne_u32_e32 vcc, 0, v4
	s_cbranch_vccnz .LBB0_937
	v_readlane_b32 s4, v254, 0
	v_readlane_b32 s5, v254, 1
	s_load_dwordx2 s[2:3], s[4:5], 0x4
	s_add_u32 s4, s96, 0x4200
	s_addc_u32 s5, s97, 0
	s_add_u32 s6, s96, 0x4400
	s_addc_u32 s7, s97, 0
	s_add_u32 s8, s96, 0x4500
	s_addc_u32 s9, s97, 0
	s_add_u32 s10, s96, 0x4600
	s_addc_u32 s11, s97, 0
	s_add_u32 s12, s96, 0x4700
	s_addc_u32 s13, s97, 0
	s_add_u32 s14, s96, 0x4800
	s_addc_u32 s15, s97, 0
	s_add_u32 s16, s96, 0x4900
	s_addc_u32 s17, s97, 0
	s_add_u32 s18, s96, 0x4a00
	s_addc_u32 s19, s97, 0
	s_add_u32 s20, s96, 0x4b00
	s_addc_u32 s21, s97, 0
	s_add_u32 s22, s96, 0x4c00
	s_addc_u32 s23, s97, 0
	s_add_u32 s24, s96, 0x4d00
	s_addc_u32 s25, s97, 0
	s_add_u32 s26, s96, 0x4e00
	s_addc_u32 s27, s97, 0
	s_add_u32 s28, s96, 0x4f00
	s_addc_u32 s29, s97, 0
	s_add_u32 s30, s96, 0x5000
	s_addc_u32 s31, s97, 0
	s_add_u32 s34, s96, 0x5100
	s_addc_u32 s35, s97, 0
	s_add_u32 s36, s96, 0x5200
	s_addc_u32 s37, s97, 0
	s_waitcnt lgkmcnt(0)
	s_mul_i32 s2, s2, s72
	s_add_u32 s38, s96, 0x5300
	s_mul_i32 s2, s2, s3
	s_addc_u32 s39, s97, 0
	s_mov_b32 s3, 1
	v_mov_b32_e32 v18, 0
	s_branch .LBB0_925
